# MLP1 GELU-output stores use sc1 (write-through) so less dirty L2 data is left for the kernel boundary
# speedup vs baseline: 1.0072x; 1.0066x over previous
.LBB5_42:
	s_mul_i32 s40, s74, 0xc00
	s_add_i32 s40, s40, 0
	v_lshl_add_u32 v135, s73, 7, v111
	s_add_i32 s44, s40, 0x24000
	s_waitcnt lgkmcnt(0)
	v_mad_i64_i32 v[96:97], s[42:43], v135, s63, 0
	v_lshl_add_u64 v[126:127], v[96:97], 1, s[8:9]
	v_add_u32_e32 v96, s44, v129
	v_lshl_add_u32 v32, v110, 2, s44
	v_add_u32_e32 v136, 0x800, v96
	ds_read_b128 v[68:71], v32
	ds_read_b128 v[60:63], v32 offset:16
	ds_read_b128 v[64:67], v32 offset:1024
	ds_read_b128 v[56:59], v32 offset:1040
	ds_read_b128 v[44:47], v32 offset:512
	ds_read_b128 v[36:39], v32 offset:528
	ds_read_b128 v[40:43], v32 offset:1536
	ds_read_b128 v[32:35], v32 offset:1552
	ds_read2_b64 v[96:99], v136 offset1:16
	s_lshl_b32 s40, s72, 8
	s_ashr_i32 s41, s40, 31
	s_lshl_b64 s[40:41], s[40:41], 1
	v_lshl_add_u64 v[126:127], v[126:127], 0, s[40:41]
	s_waitcnt lgkmcnt(0)
	v_pk_fma_f32 v[138:139], v[68:69], v[96:97], v[92:93] op_sel_hi:[1,0,1] neg_lo:[1,0,0] neg_hi:[1,0,0]
	v_xor_b32_e32 v93, 0x80000000, v71
	v_xor_b32_e32 v92, 0x80000000, v70
	v_pk_fma_f32 v[70:71], v[92:93], v[96:97], v[94:95] op_sel_hi:[1,0,1]
	v_pk_fma_f32 v[138:139], v[96:97], v[138:139], v[64:65] op_sel:[1,0,0]
	v_pk_fma_f32 v[94:95], v[96:97], v[70:71], v[66:67] op_sel:[1,0,0]
	v_xor_b32_e32 v71, 0x80000000, v63
	v_xor_b32_e32 v70, 0x80000000, v62
	v_pk_fma_f32 v[62:63], v[70:71], v[96:97], v[90:91] op_sel_hi:[1,0,1]
	v_and_b32_e32 v91, 0x7fffffff, v139
	v_and_b32_e32 v90, 0x7fffffff, v138
	v_pk_fma_f32 v[90:91], v[90:91], s[18:19], 1.0 op_sel_hi:[1,0,0]
	v_pk_fma_f32 v[140:141], v[96:97], v[62:63], v[58:59] op_sel:[1,0,0]
	v_rcp_f32_e32 v90, v90
	v_rcp_f32_e32 v91, v91
	v_mov_b64_e32 v[62:63], s[28:29]
	v_pk_mul_f32 v[144:145], v[138:139], v[138:139]
	v_cmp_gt_f32_e32 vcc, 0, v138
	v_pk_fma_f32 v[142:143], v[90:91], s[26:27], v[62:63] op_sel_hi:[1,0,0]
	v_pk_mul_f32 v[144:145], v[144:145], s[38:39] op_sel_hi:[1,0]
	v_pk_fma_f32 v[142:143], v[90:91], v[142:143], s[30:31] op_sel_hi:[1,1,0]
	v_exp_f32_e32 v144, v144
	v_exp_f32_e32 v145, v145
	v_pk_fma_f32 v[142:143], v[90:91], v[142:143], s[34:35] op_sel_hi:[1,1,0]
	v_pk_fma_f32 v[88:89], v[60:61], v[96:97], v[88:89] op_sel_hi:[1,0,1] neg_lo:[1,0,0] neg_hi:[1,0,0]
	v_pk_fma_f32 v[142:143], v[90:91], v[142:143], s[36:37] op_sel_hi:[1,1,0]
	v_pk_fma_f32 v[88:89], v[96:97], v[88:89], v[56:57] op_sel:[1,0,0]
	v_pk_mul_f32 v[90:91], v[90:91], v[142:143]
	v_pk_mul_f32 v[142:143], v[94:95], v[94:95]
	v_pk_mul_f32 v[90:91], v[144:145], v[90:91]
	v_and_b32_e32 v145, 0x7fffffff, v95
	v_and_b32_e32 v144, 0x7fffffff, v94
	v_pk_fma_f32 v[144:145], v[144:145], s[18:19], 1.0 op_sel_hi:[1,0,0]
	v_pk_mul_f32 v[146:147], v[138:139], v[90:91]
	v_rcp_f32_e32 v144, v144
	v_rcp_f32_e32 v145, v145
	v_pk_fma_f32 v[90:91], v[138:139], v[90:91], v[138:139] neg_lo:[1,0,0] neg_hi:[1,0,0]
	v_lshlrev_b32_e32 v108, 1, v110
	v_cndmask_b32_e32 v137, v90, v146, vcc
	v_cmp_gt_f32_e32 vcc, 0, v139
	v_pk_mul_f32 v[138:139], v[142:143], s[38:39] op_sel_hi:[1,0]
	v_and_b32_e32 v143, 0x7fffffff, v89
	v_cndmask_b32_e32 v146, v91, v147, vcc
	v_pk_fma_f32 v[90:91], v[144:145], s[26:27], v[62:63] op_sel_hi:[1,0,0]
	v_exp_f32_e32 v138, v138
	v_pk_fma_f32 v[90:91], v[144:145], v[90:91], s[30:31] op_sel_hi:[1,1,0]
	v_exp_f32_e32 v139, v139
	v_pk_fma_f32 v[90:91], v[144:145], v[90:91], s[34:35] op_sel_hi:[1,1,0]
	v_and_b32_e32 v142, 0x7fffffff, v88
	v_pk_fma_f32 v[90:91], v[144:145], v[90:91], s[36:37] op_sel_hi:[1,1,0]
	v_pk_fma_f32 v[142:143], v[142:143], s[18:19], 1.0 op_sel_hi:[1,0,0]
	v_pk_mul_f32 v[90:91], v[144:145], v[90:91]
	v_rcp_f32_e32 v142, v142
	v_rcp_f32_e32 v143, v143
	v_pk_mul_f32 v[90:91], v[138:139], v[90:91]
	v_cmp_gt_f32_e32 vcc, 0, v94
	v_pk_mul_f32 v[138:139], v[94:95], v[90:91]
	v_pk_fma_f32 v[90:91], v[94:95], v[90:91], v[94:95] neg_lo:[1,0,0] neg_hi:[1,0,0]
	v_lshl_add_u64 v[126:127], v[126:127], 0, v[108:109]
	v_cndmask_b32_e32 v144, v90, v138, vcc
	v_cmp_gt_f32_e32 vcc, 0, v95
	v_pk_mul_f32 v[94:95], v[88:89], v[88:89]
	v_xor_b32_e32 v39, 0x80000000, v39
	v_cndmask_b32_e32 v145, v91, v139, vcc
	v_pk_fma_f32 v[90:91], v[142:143], s[26:27], v[62:63] op_sel_hi:[1,0,0]
	v_pk_mul_f32 v[94:95], v[94:95], s[38:39] op_sel_hi:[1,0]
	v_pk_fma_f32 v[90:91], v[142:143], v[90:91], s[30:31] op_sel_hi:[1,1,0]
	v_exp_f32_e32 v94, v94
	v_exp_f32_e32 v95, v95
	v_pk_fma_f32 v[90:91], v[142:143], v[90:91], s[34:35] op_sel_hi:[1,1,0]
	v_cmp_gt_f32_e32 vcc, 0, v88
	v_pk_fma_f32 v[90:91], v[142:143], v[90:91], s[36:37] op_sel_hi:[1,1,0]
	v_pk_mul_f32 v[138:139], v[140:141], v[140:141]
	v_pk_mul_f32 v[90:91], v[142:143], v[90:91]
	v_xor_b32_e32 v38, 0x80000000, v38
	v_pk_mul_f32 v[90:91], v[94:95], v[90:91]
	v_and_b32_e32 v95, 0x7fffffff, v141
	v_and_b32_e32 v94, 0x7fffffff, v140
	v_pk_fma_f32 v[94:95], v[94:95], s[18:19], 1.0 op_sel_hi:[1,0,0]
	v_pk_mul_f32 v[142:143], v[88:89], v[90:91]
	v_rcp_f32_e32 v94, v94
	v_rcp_f32_e32 v95, v95
	v_pk_fma_f32 v[90:91], v[88:89], v[90:91], v[88:89] neg_lo:[1,0,0] neg_hi:[1,0,0]
	v_pk_fma_f32 v[80:81], v[36:37], v[96:97], v[80:81] op_sel_hi:[1,0,1] neg_lo:[1,0,0] neg_hi:[1,0,0]
	v_cndmask_b32_e32 v142, v90, v142, vcc
	v_cmp_gt_f32_e32 vcc, 0, v89
	v_pk_fma_f32 v[88:89], v[94:95], s[26:27], v[62:63] op_sel_hi:[1,0,0]
	v_pk_fma_f32 v[82:83], v[38:39], v[96:97], v[82:83] op_sel_hi:[1,0,1]
	v_cndmask_b32_e32 v143, v91, v143, vcc
	v_pk_mul_f32 v[90:91], v[138:139], s[38:39] op_sel_hi:[1,0]
	v_pk_fma_f32 v[88:89], v[94:95], v[88:89], s[30:31] op_sel_hi:[1,1,0]
	v_exp_f32_e32 v90, v90
	v_exp_f32_e32 v91, v91
	v_pk_fma_f32 v[88:89], v[94:95], v[88:89], s[34:35] op_sel_hi:[1,1,0]
	v_cmp_gt_f32_e32 vcc, 0, v140
	v_pk_fma_f32 v[88:89], v[94:95], v[88:89], s[36:37] op_sel_hi:[1,1,0]
	v_pk_fma_f32 v[82:83], v[96:97], v[82:83], v[34:35] op_sel:[1,0,0]
	v_pk_mul_f32 v[88:89], v[94:95], v[88:89]
	v_pk_fma_f32 v[80:81], v[96:97], v[80:81], v[32:33] op_sel:[1,0,0]
	v_pk_mul_f32 v[88:89], v[90:91], v[88:89]
	v_pk_fma_f32 v[76:77], v[68:69], v[98:99], v[76:77] op_sel_hi:[1,0,1] neg_lo:[1,0,0] neg_hi:[1,0,0]
	v_pk_mul_f32 v[90:91], v[140:141], v[88:89]
	v_pk_fma_f32 v[88:89], v[140:141], v[88:89], v[140:141] neg_lo:[1,0,0] neg_hi:[1,0,0]
	v_pk_fma_f32 v[76:77], v[98:99], v[76:77], v[64:65] op_sel:[1,0,0]
	v_cndmask_b32_e32 v94, v88, v90, vcc
	v_cmp_gt_f32_e32 vcc, 0, v141
	v_cvt_pk_f16_f32 v88, v137, v146
	v_cvt_pk_f16_f32 v90, v142, v143
	v_cndmask_b32_e32 v91, v89, v91, vcc
	v_cvt_pk_f16_f32 v89, v144, v145
	v_cvt_pk_f16_f32 v91, v94, v91
	global_store_dwordx4 v[126:127], v[88:91], off sc1
	v_pk_fma_f32 v[78:79], v[92:93], v[98:99], v[78:79] op_sel_hi:[1,0,1]
	v_pk_fma_f32 v[72:73], v[60:61], v[98:99], v[72:73] op_sel_hi:[1,0,1] neg_lo:[1,0,0] neg_hi:[1,0,0]
	v_pk_fma_f32 v[88:89], v[44:45], v[96:97], v[84:85] op_sel_hi:[1,0,1] neg_lo:[1,0,0] neg_hi:[1,0,0]
	v_xor_b32_e32 v85, 0x80000000, v47
	v_xor_b32_e32 v84, 0x80000000, v46
	v_pk_fma_f32 v[46:47], v[84:85], v[96:97], v[86:87] op_sel_hi:[1,0,1]
	v_pk_fma_f32 v[86:87], v[96:97], v[88:89], v[40:41] op_sel:[1,0,0]
	v_pk_fma_f32 v[46:47], v[96:97], v[46:47], v[42:43] op_sel:[1,0,0]
	v_and_b32_e32 v89, 0x7fffffff, v87
	v_and_b32_e32 v88, 0x7fffffff, v86
	v_pk_fma_f32 v[88:89], v[88:89], s[18:19], 1.0 op_sel_hi:[1,0,0]
	v_pk_mul_f32 v[94:95], v[86:87], v[86:87]
	v_rcp_f32_e32 v88, v88
	v_rcp_f32_e32 v89, v89
	v_pk_mul_f32 v[94:95], v[94:95], s[38:39] op_sel_hi:[1,0]
	v_and_b32_e32 v97, 0x7fffffff, v47
	v_exp_f32_e32 v94, v94
	v_pk_fma_f32 v[90:91], v[88:89], s[26:27], v[62:63] op_sel_hi:[1,0,0]
	v_exp_f32_e32 v95, v95
	v_pk_fma_f32 v[90:91], v[88:89], v[90:91], s[30:31] op_sel_hi:[1,1,0]
	v_and_b32_e32 v96, 0x7fffffff, v46
	v_pk_fma_f32 v[90:91], v[88:89], v[90:91], s[34:35] op_sel_hi:[1,1,0]
	v_pk_fma_f32 v[96:97], v[96:97], s[18:19], 1.0 op_sel_hi:[1,0,0]
	v_pk_fma_f32 v[90:91], v[88:89], v[90:91], s[36:37] op_sel_hi:[1,1,0]
	v_rcp_f32_e32 v96, v96
	v_pk_mul_f32 v[88:89], v[88:89], v[90:91]
	v_rcp_f32_e32 v97, v97
	v_pk_mul_f32 v[88:89], v[94:95], v[88:89]
	v_cmp_gt_f32_e32 vcc, 0, v86
	v_pk_mul_f32 v[94:95], v[86:87], v[88:89]
	v_pk_fma_f32 v[88:89], v[86:87], v[88:89], v[86:87] neg_lo:[1,0,0] neg_hi:[1,0,0]
	v_pk_mul_f32 v[90:91], v[46:47], v[46:47]
	v_cndmask_b32_e32 v94, v88, v94, vcc
	v_cmp_gt_f32_e32 vcc, 0, v87
	v_pk_fma_f32 v[86:87], v[96:97], s[26:27], v[62:63] op_sel_hi:[1,0,0]
	v_pk_fma_f32 v[78:79], v[98:99], v[78:79], v[66:67] op_sel:[1,0,0]
	v_cndmask_b32_e32 v95, v89, v95, vcc
	v_pk_mul_f32 v[88:89], v[90:91], s[38:39] op_sel_hi:[1,0]
	v_pk_fma_f32 v[86:87], v[96:97], v[86:87], s[30:31] op_sel_hi:[1,1,0]
	v_exp_f32_e32 v88, v88
	v_exp_f32_e32 v89, v89
	v_and_b32_e32 v91, 0x7fffffff, v81
	v_and_b32_e32 v90, 0x7fffffff, v80
	v_pk_fma_f32 v[86:87], v[96:97], v[86:87], s[34:35] op_sel_hi:[1,1,0]
	v_pk_fma_f32 v[90:91], v[90:91], s[18:19], 1.0 op_sel_hi:[1,0,0]
	v_pk_fma_f32 v[86:87], v[96:97], v[86:87], s[36:37] op_sel_hi:[1,1,0]
	v_rcp_f32_e32 v90, v90
	v_rcp_f32_e32 v91, v91
	v_pk_mul_f32 v[86:87], v[96:97], v[86:87]
	v_cmp_gt_f32_e32 vcc, 0, v46
	v_pk_mul_f32 v[86:87], v[88:89], v[86:87]
	v_pk_fma_f32 v[72:73], v[98:99], v[72:73], v[56:57] op_sel:[1,0,0]
	v_pk_mul_f32 v[88:89], v[46:47], v[86:87]
	v_pk_fma_f32 v[86:87], v[46:47], v[86:87], v[46:47] neg_lo:[1,0,0] neg_hi:[1,0,0]
	v_pk_fma_f32 v[74:75], v[70:71], v[98:99], v[74:75] op_sel_hi:[1,0,1]
	v_cndmask_b32_e32 v96, v86, v88, vcc
	v_cmp_gt_f32_e32 vcc, 0, v47
	v_pk_fma_f32 v[46:47], v[90:91], s[26:27], v[62:63] op_sel_hi:[1,0,0]
	v_pk_fma_f32 v[74:75], v[98:99], v[74:75], v[58:59] op_sel:[1,0,0]
	v_cndmask_b32_e32 v97, v87, v89, vcc
	v_pk_fma_f32 v[46:47], v[90:91], v[46:47], s[30:31] op_sel_hi:[1,1,0]
	v_pk_mul_f32 v[86:87], v[80:81], v[80:81]
	v_pk_fma_f32 v[46:47], v[90:91], v[46:47], s[34:35] op_sel_hi:[1,1,0]
	v_pk_mul_f32 v[86:87], v[86:87], s[38:39] op_sel_hi:[1,0]
	v_pk_fma_f32 v[46:47], v[90:91], v[46:47], s[36:37] op_sel_hi:[1,1,0]
	v_exp_f32_e32 v86, v86
	v_exp_f32_e32 v87, v87
	v_pk_mul_f32 v[46:47], v[90:91], v[46:47]
	v_and_b32_e32 v91, 0x7fffffff, v83
	v_and_b32_e32 v90, 0x7fffffff, v82
	v_pk_fma_f32 v[90:91], v[90:91], s[18:19], 1.0 op_sel_hi:[1,0,0]
	v_pk_mul_f32 v[46:47], v[86:87], v[46:47]
	v_rcp_f32_e32 v90, v90
	v_rcp_f32_e32 v91, v91
	v_pk_mul_f32 v[86:87], v[80:81], v[46:47]
	v_pk_fma_f32 v[46:47], v[80:81], v[46:47], v[80:81] neg_lo:[1,0,0] neg_hi:[1,0,0]
	v_cmp_gt_f32_e32 vcc, 0, v80
	v_pk_mul_f32 v[88:89], v[82:83], v[82:83]
	v_pk_fma_f32 v[52:53], v[44:45], v[98:99], v[52:53] op_sel_hi:[1,0,1] neg_lo:[1,0,0] neg_hi:[1,0,0]
	v_cndmask_b32_e32 v86, v46, v86, vcc
	v_cmp_gt_f32_e32 vcc, 0, v81
	v_pk_mul_f32 v[80:81], v[88:89], s[38:39] op_sel_hi:[1,0]
	v_and_b32_e32 v89, 0x7fffffff, v79
	v_cndmask_b32_e32 v87, v47, v87, vcc
	v_pk_fma_f32 v[46:47], v[90:91], s[26:27], v[62:63] op_sel_hi:[1,0,0]
	v_exp_f32_e32 v80, v80
	v_pk_fma_f32 v[46:47], v[90:91], v[46:47], s[30:31] op_sel_hi:[1,1,0]
	v_exp_f32_e32 v81, v81
	v_pk_fma_f32 v[46:47], v[90:91], v[46:47], s[34:35] op_sel_hi:[1,1,0]
	v_cmp_gt_f32_e32 vcc, 0, v82
	v_pk_fma_f32 v[46:47], v[90:91], v[46:47], s[36:37] op_sel_hi:[1,1,0]
	v_and_b32_e32 v88, 0x7fffffff, v78
	v_pk_mul_f32 v[46:47], v[90:91], v[46:47]
	v_pk_fma_f32 v[88:89], v[88:89], s[18:19], 1.0 op_sel_hi:[1,0,0]
	v_pk_mul_f32 v[46:47], v[80:81], v[46:47]
	v_rcp_f32_e32 v88, v88
	v_pk_mul_f32 v[80:81], v[82:83], v[46:47]
	v_pk_fma_f32 v[46:47], v[82:83], v[46:47], v[82:83] neg_lo:[1,0,0] neg_hi:[1,0,0]
	v_cvt_pk_f16_f32 v82, v86, v87
	v_cndmask_b32_e32 v46, v46, v80, vcc
	v_cmp_gt_f32_e32 vcc, 0, v83
	v_cvt_pk_f16_f32 v80, v94, v95
	v_pk_mul_f32 v[86:87], v[76:77], v[76:77]
	v_cndmask_b32_e32 v47, v47, v81, vcc
	v_cvt_pk_f16_f32 v81, v96, v97
	v_cvt_pk_f16_f32 v83, v46, v47
	global_store_dwordx4 v[126:127], v[80:83], off offset:256 sc1
	v_pk_mul_f32 v[86:87], v[86:87], s[38:39] op_sel_hi:[1,0]
	v_rcp_f32_e32 v89, v89
	v_and_b32_e32 v81, 0x7fffffff, v77
	v_and_b32_e32 v80, 0x7fffffff, v76
	v_pk_fma_f32 v[80:81], v[80:81], s[18:19], 1.0 op_sel_hi:[1,0,0]
	v_exp_f32_e32 v86, v86
	v_rcp_f32_e32 v80, v80
	v_rcp_f32_e32 v81, v81
	v_exp_f32_e32 v87, v87
	v_cmp_gt_f32_e32 vcc, 0, v76
	v_or_b32_e32 v46, 16, v135
	v_pk_fma_f32 v[82:83], v[80:81], s[26:27], v[62:63] op_sel_hi:[1,0,0]
	v_mad_i64_i32 v[46:47], s[42:43], v46, s63, 0
	v_pk_fma_f32 v[82:83], v[80:81], v[82:83], s[30:31] op_sel_hi:[1,1,0]
	v_lshl_add_u64 v[46:47], v[46:47], 1, s[8:9]
	v_pk_fma_f32 v[82:83], v[80:81], v[82:83], s[34:35] op_sel_hi:[1,1,0]
	v_lshl_add_u64 v[46:47], v[46:47], 0, s[40:41]
	v_pk_fma_f32 v[82:83], v[80:81], v[82:83], s[36:37] op_sel_hi:[1,1,0]
	v_lshl_add_u64 v[46:47], v[46:47], 0, v[108:109]
	v_pk_mul_f32 v[80:81], v[80:81], v[82:83]
	v_pk_mul_f32 v[82:83], v[78:79], v[78:79]
	v_pk_mul_f32 v[80:81], v[86:87], v[80:81]
	v_pk_fma_f32 v[52:53], v[98:99], v[52:53], v[40:41] op_sel:[1,0,0]
	v_pk_mul_f32 v[86:87], v[76:77], v[80:81]
	v_pk_fma_f32 v[80:81], v[76:77], v[80:81], v[76:77] neg_lo:[1,0,0] neg_hi:[1,0,0]
	v_pk_fma_f32 v[54:55], v[84:85], v[98:99], v[54:55] op_sel_hi:[1,0,1]
	v_cndmask_b32_e32 v86, v80, v86, vcc
	v_cmp_gt_f32_e32 vcc, 0, v77
	v_pk_fma_f32 v[76:77], v[88:89], s[26:27], v[62:63] op_sel_hi:[1,0,0]
	v_pk_fma_f32 v[54:55], v[98:99], v[54:55], v[42:43] op_sel:[1,0,0]
	v_cndmask_b32_e32 v87, v81, v87, vcc
	v_pk_mul_f32 v[80:81], v[82:83], s[38:39] op_sel_hi:[1,0]
	v_pk_fma_f32 v[76:77], v[88:89], v[76:77], s[30:31] op_sel_hi:[1,1,0]
	v_exp_f32_e32 v80, v80
	v_exp_f32_e32 v81, v81
	v_pk_fma_f32 v[76:77], v[88:89], v[76:77], s[34:35] op_sel_hi:[1,1,0]
	v_and_b32_e32 v83, 0x7fffffff, v73
	v_and_b32_e32 v82, 0x7fffffff, v72
	v_pk_fma_f32 v[76:77], v[88:89], v[76:77], s[36:37] op_sel_hi:[1,1,0]
	v_pk_fma_f32 v[82:83], v[82:83], s[18:19], 1.0 op_sel_hi:[1,0,0]
	v_pk_mul_f32 v[76:77], v[88:89], v[76:77]
	v_rcp_f32_e32 v82, v82
	v_rcp_f32_e32 v83, v83
	v_pk_mul_f32 v[76:77], v[80:81], v[76:77]
	v_cmp_gt_f32_e32 vcc, 0, v78
	v_pk_mul_f32 v[80:81], v[78:79], v[76:77]
	v_pk_fma_f32 v[76:77], v[78:79], v[76:77], v[78:79] neg_lo:[1,0,0] neg_hi:[1,0,0]
	v_pk_fma_f32 v[48:49], v[36:37], v[98:99], v[48:49] op_sel_hi:[1,0,1] neg_lo:[1,0,0] neg_hi:[1,0,0]
	v_cndmask_b32_e32 v88, v76, v80, vcc
	v_cmp_gt_f32_e32 vcc, 0, v79
	v_pk_mul_f32 v[78:79], v[72:73], v[72:73]
	v_pk_fma_f32 v[48:49], v[98:99], v[48:49], v[32:33] op_sel:[1,0,0]
	v_cndmask_b32_e32 v89, v77, v81, vcc
	v_pk_fma_f32 v[76:77], v[82:83], s[26:27], v[62:63] op_sel_hi:[1,0,0]
	v_pk_mul_f32 v[78:79], v[78:79], s[38:39] op_sel_hi:[1,0]
	v_pk_fma_f32 v[76:77], v[82:83], v[76:77], s[30:31] op_sel_hi:[1,1,0]
	v_exp_f32_e32 v78, v78
	v_pk_fma_f32 v[76:77], v[82:83], v[76:77], s[34:35] op_sel_hi:[1,1,0]
	v_exp_f32_e32 v79, v79
	v_pk_fma_f32 v[76:77], v[82:83], v[76:77], s[36:37] op_sel_hi:[1,1,0]
	v_cmp_gt_f32_e32 vcc, 0, v72
	v_pk_mul_f32 v[76:77], v[82:83], v[76:77]
	v_and_b32_e32 v83, 0x7fffffff, v75
	v_and_b32_e32 v82, 0x7fffffff, v74
	v_pk_fma_f32 v[82:83], v[82:83], s[18:19], 1.0 op_sel_hi:[1,0,0]
	v_pk_mul_f32 v[76:77], v[78:79], v[76:77]
	v_rcp_f32_e32 v82, v82
	v_rcp_f32_e32 v83, v83
	v_pk_mul_f32 v[78:79], v[72:73], v[76:77]
	v_pk_fma_f32 v[76:77], v[72:73], v[76:77], v[72:73] neg_lo:[1,0,0] neg_hi:[1,0,0]
	v_pk_mul_f32 v[80:81], v[74:75], v[74:75]
	v_cndmask_b32_e32 v78, v76, v78, vcc
	v_cmp_gt_f32_e32 vcc, 0, v73
	v_pk_fma_f32 v[72:73], v[82:83], s[26:27], v[62:63] op_sel_hi:[1,0,0]
	v_pk_fma_f32 v[50:51], v[38:39], v[98:99], v[50:51] op_sel_hi:[1,0,1]
	v_cndmask_b32_e32 v79, v77, v79, vcc
	v_pk_mul_f32 v[76:77], v[80:81], s[38:39] op_sel_hi:[1,0]
	v_pk_fma_f32 v[72:73], v[82:83], v[72:73], s[30:31] op_sel_hi:[1,1,0]
	v_exp_f32_e32 v76, v76
	v_exp_f32_e32 v77, v77
	v_pk_fma_f32 v[72:73], v[82:83], v[72:73], s[34:35] op_sel_hi:[1,1,0]
	v_cmp_gt_f32_e32 vcc, 0, v74
	v_pk_fma_f32 v[72:73], v[82:83], v[72:73], s[36:37] op_sel_hi:[1,1,0]
	v_pk_fma_f32 v[50:51], v[98:99], v[50:51], v[34:35] op_sel:[1,0,0]
	v_pk_mul_f32 v[72:73], v[82:83], v[72:73]
	s_mov_b32 s72, s70
	v_pk_mul_f32 v[72:73], v[76:77], v[72:73]
	s_mov_b32 s73, s71
	v_pk_mul_f32 v[76:77], v[74:75], v[72:73]
	v_pk_fma_f32 v[72:73], v[74:75], v[72:73], v[74:75] neg_lo:[1,0,0] neg_hi:[1,0,0]
	v_cvt_pk_f16_f32 v74, v78, v79
	v_cndmask_b32_e32 v76, v72, v76, vcc
	v_cmp_gt_f32_e32 vcc, 0, v75
	v_cvt_pk_f16_f32 v72, v86, v87
	v_and_b32_e32 v79, 0x7fffffff, v55
	v_cndmask_b32_e32 v75, v73, v77, vcc
	v_cvt_pk_f16_f32 v73, v88, v89
	v_cvt_pk_f16_f32 v75, v76, v75
	global_store_dwordx4 v[46:47], v[72:75], off sc1
	v_pk_mul_f32 v[76:77], v[52:53], v[52:53]
	v_and_b32_e32 v78, 0x7fffffff, v54
	v_and_b32_e32 v73, 0x7fffffff, v53
	v_and_b32_e32 v72, 0x7fffffff, v52
	v_pk_fma_f32 v[72:73], v[72:73], s[18:19], 1.0 op_sel_hi:[1,0,0]
	v_pk_mul_f32 v[76:77], v[76:77], s[38:39] op_sel_hi:[1,0]
	v_rcp_f32_e32 v72, v72
	v_rcp_f32_e32 v73, v73
	v_exp_f32_e32 v76, v76
	v_exp_f32_e32 v77, v77
	v_pk_fma_f32 v[78:79], v[78:79], s[18:19], 1.0 op_sel_hi:[1,0,0]
	v_pk_fma_f32 v[74:75], v[72:73], s[26:27], v[62:63] op_sel_hi:[1,0,0]
	v_rcp_f32_e32 v78, v78
	v_pk_fma_f32 v[74:75], v[72:73], v[74:75], s[30:31] op_sel_hi:[1,1,0]
	v_rcp_f32_e32 v79, v79
	v_pk_fma_f32 v[74:75], v[72:73], v[74:75], s[34:35] op_sel_hi:[1,1,0]
	v_cmp_gt_f32_e32 vcc, 0, v52
	v_pk_fma_f32 v[74:75], v[72:73], v[74:75], s[36:37] op_sel_hi:[1,1,0]
	s_mov_b32 s74, s69
	v_pk_mul_f32 v[72:73], v[72:73], v[74:75]
	v_pk_mul_f32 v[74:75], v[54:55], v[54:55]
	v_pk_mul_f32 v[72:73], v[76:77], v[72:73]
	s_nop 0
	v_pk_mul_f32 v[76:77], v[52:53], v[72:73]
	v_pk_fma_f32 v[72:73], v[52:53], v[72:73], v[52:53] neg_lo:[1,0,0] neg_hi:[1,0,0]
	s_nop 0
	v_cndmask_b32_e32 v76, v72, v76, vcc
	v_cmp_gt_f32_e32 vcc, 0, v53
	v_pk_fma_f32 v[52:53], v[78:79], s[26:27], v[62:63] op_sel_hi:[1,0,0]
	s_nop 0
	v_cndmask_b32_e32 v77, v73, v77, vcc
	v_pk_mul_f32 v[72:73], v[74:75], s[38:39] op_sel_hi:[1,0]
	v_pk_fma_f32 v[52:53], v[78:79], v[52:53], s[30:31] op_sel_hi:[1,1,0]
	v_exp_f32_e32 v72, v72
	v_exp_f32_e32 v73, v73
	v_pk_fma_f32 v[52:53], v[78:79], v[52:53], s[34:35] op_sel_hi:[1,1,0]
	v_and_b32_e32 v75, 0x7fffffff, v49
	v_and_b32_e32 v74, 0x7fffffff, v48
	v_pk_fma_f32 v[52:53], v[78:79], v[52:53], s[36:37] op_sel_hi:[1,1,0]
	v_pk_fma_f32 v[74:75], v[74:75], s[18:19], 1.0 op_sel_hi:[1,0,0]
	v_pk_mul_f32 v[52:53], v[78:79], v[52:53]
	v_rcp_f32_e32 v74, v74
	v_rcp_f32_e32 v75, v75
	v_pk_mul_f32 v[52:53], v[72:73], v[52:53]
	v_cmp_gt_f32_e32 vcc, 0, v54
	v_pk_mul_f32 v[72:73], v[54:55], v[52:53]
	v_pk_fma_f32 v[52:53], v[54:55], v[52:53], v[54:55] neg_lo:[1,0,0] neg_hi:[1,0,0]
	s_nop 0
	v_cndmask_b32_e32 v78, v52, v72, vcc
	v_cmp_gt_f32_e32 vcc, 0, v55
	v_pk_mul_f32 v[54:55], v[48:49], v[48:49]
	s_nop 0
	v_cndmask_b32_e32 v79, v53, v73, vcc
	v_pk_fma_f32 v[52:53], v[74:75], s[26:27], v[62:63] op_sel_hi:[1,0,0]
	v_pk_mul_f32 v[54:55], v[54:55], s[38:39] op_sel_hi:[1,0]
	v_pk_fma_f32 v[52:53], v[74:75], v[52:53], s[30:31] op_sel_hi:[1,1,0]
	v_exp_f32_e32 v54, v54
	v_pk_fma_f32 v[52:53], v[74:75], v[52:53], s[34:35] op_sel_hi:[1,1,0]
	v_exp_f32_e32 v55, v55
	v_pk_fma_f32 v[52:53], v[74:75], v[52:53], s[36:37] op_sel_hi:[1,1,0]
	v_cmp_gt_f32_e32 vcc, 0, v48
	v_pk_mul_f32 v[52:53], v[74:75], v[52:53]
	v_and_b32_e32 v75, 0x7fffffff, v51
	v_and_b32_e32 v74, 0x7fffffff, v50
	v_pk_fma_f32 v[74:75], v[74:75], s[18:19], 1.0 op_sel_hi:[1,0,0]
	v_pk_mul_f32 v[52:53], v[54:55], v[52:53]
	v_rcp_f32_e32 v74, v74
	v_rcp_f32_e32 v75, v75
	v_pk_mul_f32 v[54:55], v[48:49], v[52:53]
	v_pk_fma_f32 v[52:53], v[48:49], v[52:53], v[48:49] neg_lo:[1,0,0] neg_hi:[1,0,0]
	v_pk_mul_f32 v[72:73], v[50:51], v[50:51]
	v_cndmask_b32_e32 v54, v52, v54, vcc
	v_cmp_gt_f32_e32 vcc, 0, v49
	v_pk_fma_f32 v[48:49], v[74:75], s[26:27], v[62:63] op_sel_hi:[1,0,0]
	s_nop 0
	v_cndmask_b32_e32 v55, v53, v55, vcc
	v_pk_mul_f32 v[52:53], v[72:73], s[38:39] op_sel_hi:[1,0]
	v_pk_fma_f32 v[48:49], v[74:75], v[48:49], s[30:31] op_sel_hi:[1,1,0]
	v_exp_f32_e32 v52, v52
	v_exp_f32_e32 v53, v53
	v_pk_fma_f32 v[48:49], v[74:75], v[48:49], s[34:35] op_sel_hi:[1,1,0]
	v_cmp_gt_f32_e32 vcc, 0, v50
	v_pk_fma_f32 v[48:49], v[74:75], v[48:49], s[36:37] op_sel_hi:[1,1,0]
	s_nop 0
	v_pk_mul_f32 v[48:49], v[74:75], v[48:49]
	s_nop 0
	v_pk_mul_f32 v[48:49], v[52:53], v[48:49]
	s_nop 0
	v_pk_mul_f32 v[52:53], v[50:51], v[48:49]
	v_pk_fma_f32 v[48:49], v[50:51], v[48:49], v[50:51] neg_lo:[1,0,0] neg_hi:[1,0,0]
	v_cvt_pk_f16_f32 v50, v54, v55
	v_cndmask_b32_e32 v52, v48, v52, vcc
	v_cmp_gt_f32_e32 vcc, 0, v51
	v_cvt_pk_f16_f32 v48, v76, v77
	s_nop 0
	v_cndmask_b32_e32 v51, v49, v53, vcc
	v_cvt_pk_f16_f32 v49, v78, v79
	v_cvt_pk_f16_f32 v51, v52, v51
	global_store_dwordx4 v[46:47], v[48:51], off offset:256 sc1
	ds_read2_b64 v[46:49], v136 offset0:32 offset1:48
	s_waitcnt lgkmcnt(0)
	v_pk_fma_f32 v[28:29], v[68:69], v[46:47], v[28:29] op_sel_hi:[1,0,1] neg_lo:[1,0,0] neg_hi:[1,0,0]
	s_nop 0
	v_pk_fma_f32 v[28:29], v[46:47], v[28:29], v[64:65] op_sel:[1,0,0]
	v_pk_fma_f32 v[30:31], v[92:93], v[46:47], v[30:31] op_sel_hi:[1,0,1]
	v_and_b32_e32 v53, 0x7fffffff, v29
	v_and_b32_e32 v52, 0x7fffffff, v28
	v_pk_fma_f32 v[52:53], v[52:53], s[18:19], 1.0 op_sel_hi:[1,0,0]
	v_pk_mul_f32 v[72:73], v[28:29], v[28:29]
	v_rcp_f32_e32 v52, v52
	v_rcp_f32_e32 v53, v53
	v_pk_mul_f32 v[72:73], v[72:73], s[38:39] op_sel_hi:[1,0]
	v_pk_fma_f32 v[30:31], v[46:47], v[30:31], v[66:67] op_sel:[1,0,0]
	v_exp_f32_e32 v72, v72
	v_pk_fma_f32 v[54:55], v[52:53], s[26:27], v[62:63] op_sel_hi:[1,0,0]
	v_exp_f32_e32 v73, v73
	v_pk_fma_f32 v[54:55], v[52:53], v[54:55], s[30:31] op_sel_hi:[1,1,0]
	v_and_b32_e32 v75, 0x7fffffff, v31
	v_pk_fma_f32 v[54:55], v[52:53], v[54:55], s[34:35] op_sel_hi:[1,1,0]
	v_and_b32_e32 v74, 0x7fffffff, v30
	v_pk_fma_f32 v[54:55], v[52:53], v[54:55], s[36:37] op_sel_hi:[1,1,0]
	v_pk_fma_f32 v[74:75], v[74:75], s[18:19], 1.0 op_sel_hi:[1,0,0]
	v_pk_mul_f32 v[52:53], v[52:53], v[54:55]
	v_rcp_f32_e32 v74, v74
	v_rcp_f32_e32 v75, v75
	v_pk_mul_f32 v[52:53], v[72:73], v[52:53]
	v_cmp_gt_f32_e32 vcc, 0, v28
	v_pk_mul_f32 v[72:73], v[28:29], v[52:53]
	v_pk_fma_f32 v[52:53], v[28:29], v[52:53], v[28:29] neg_lo:[1,0,0] neg_hi:[1,0,0]
	v_pk_mul_f32 v[54:55], v[30:31], v[30:31]
	v_cndmask_b32_e32 v72, v52, v72, vcc
	v_cmp_gt_f32_e32 vcc, 0, v29
	v_pk_fma_f32 v[24:25], v[60:61], v[46:47], v[24:25] op_sel_hi:[1,0,1] neg_lo:[1,0,0] neg_hi:[1,0,0]
	v_pk_fma_f32 v[28:29], v[74:75], s[26:27], v[62:63] op_sel_hi:[1,0,0]
	v_cndmask_b32_e32 v73, v53, v73, vcc
	v_pk_mul_f32 v[52:53], v[54:55], s[38:39] op_sel_hi:[1,0]
	v_pk_fma_f32 v[24:25], v[46:47], v[24:25], v[56:57] op_sel:[1,0,0]
	v_pk_fma_f32 v[28:29], v[74:75], v[28:29], s[30:31] op_sel_hi:[1,1,0]
	v_exp_f32_e32 v52, v52
	v_exp_f32_e32 v53, v53
	v_pk_fma_f32 v[28:29], v[74:75], v[28:29], s[34:35] op_sel_hi:[1,1,0]
	v_and_b32_e32 v55, 0x7fffffff, v25
	v_and_b32_e32 v54, 0x7fffffff, v24
	v_pk_fma_f32 v[28:29], v[74:75], v[28:29], s[36:37] op_sel_hi:[1,1,0]
	v_pk_fma_f32 v[54:55], v[54:55], s[18:19], 1.0 op_sel_hi:[1,0,0]
	v_pk_mul_f32 v[28:29], v[74:75], v[28:29]
	v_rcp_f32_e32 v54, v54
	v_rcp_f32_e32 v55, v55
	v_pk_mul_f32 v[28:29], v[52:53], v[28:29]
	v_cmp_gt_f32_e32 vcc, 0, v30
	v_pk_mul_f32 v[52:53], v[30:31], v[28:29]
	v_pk_fma_f32 v[28:29], v[30:31], v[28:29], v[30:31] neg_lo:[1,0,0] neg_hi:[1,0,0]
	v_pk_fma_f32 v[26:27], v[70:71], v[46:47], v[26:27] op_sel_hi:[1,0,1]
	v_cndmask_b32_e32 v74, v28, v52, vcc
	v_cmp_gt_f32_e32 vcc, 0, v31
	v_pk_mul_f32 v[30:31], v[24:25], v[24:25]
	v_pk_fma_f32 v[26:27], v[46:47], v[26:27], v[58:59] op_sel:[1,0,0]
	v_cndmask_b32_e32 v75, v29, v53, vcc
	v_pk_fma_f32 v[28:29], v[54:55], s[26:27], v[62:63] op_sel_hi:[1,0,0]
	v_pk_mul_f32 v[30:31], v[30:31], s[38:39] op_sel_hi:[1,0]
	v_pk_fma_f32 v[28:29], v[54:55], v[28:29], s[30:31] op_sel_hi:[1,1,0]
	v_exp_f32_e32 v30, v30
	v_pk_fma_f32 v[28:29], v[54:55], v[28:29], s[34:35] op_sel_hi:[1,1,0]
	v_exp_f32_e32 v31, v31
	v_pk_fma_f32 v[28:29], v[54:55], v[28:29], s[36:37] op_sel_hi:[1,1,0]
	v_cmp_gt_f32_e32 vcc, 0, v24
	v_pk_mul_f32 v[28:29], v[54:55], v[28:29]
	v_and_b32_e32 v55, 0x7fffffff, v27
	v_and_b32_e32 v54, 0x7fffffff, v26
	v_pk_fma_f32 v[54:55], v[54:55], s[18:19], 1.0 op_sel_hi:[1,0,0]
	v_pk_mul_f32 v[28:29], v[30:31], v[28:29]
	v_rcp_f32_e32 v54, v54
	v_rcp_f32_e32 v55, v55
	v_pk_mul_f32 v[30:31], v[24:25], v[28:29]
	v_pk_fma_f32 v[28:29], v[24:25], v[28:29], v[24:25] neg_lo:[1,0,0] neg_hi:[1,0,0]
	v_pk_mul_f32 v[52:53], v[26:27], v[26:27]
	v_cndmask_b32_e32 v30, v28, v30, vcc
	v_cmp_gt_f32_e32 vcc, 0, v25
	v_pk_fma_f32 v[24:25], v[54:55], s[26:27], v[62:63] op_sel_hi:[1,0,0]
	v_or_b32_e32 v50, 32, v135
	v_cndmask_b32_e32 v31, v29, v31, vcc
	v_pk_mul_f32 v[28:29], v[52:53], s[38:39] op_sel_hi:[1,0]
	v_pk_fma_f32 v[24:25], v[54:55], v[24:25], s[30:31] op_sel_hi:[1,1,0]
	v_exp_f32_e32 v28, v28
	v_exp_f32_e32 v29, v29
	v_pk_fma_f32 v[24:25], v[54:55], v[24:25], s[34:35] op_sel_hi:[1,1,0]
	v_mad_i64_i32 v[50:51], s[42:43], v50, s63, 0
	v_pk_fma_f32 v[24:25], v[54:55], v[24:25], s[36:37] op_sel_hi:[1,1,0]
	v_cmp_gt_f32_e32 vcc, 0, v26
	v_pk_mul_f32 v[24:25], v[54:55], v[24:25]
	v_lshl_add_u64 v[50:51], v[50:51], 1, s[8:9]
	v_pk_mul_f32 v[24:25], v[28:29], v[24:25]
	v_lshl_add_u64 v[50:51], v[50:51], 0, s[40:41]
	v_pk_mul_f32 v[28:29], v[26:27], v[24:25]
	v_pk_fma_f32 v[24:25], v[26:27], v[24:25], v[26:27] neg_lo:[1,0,0] neg_hi:[1,0,0]
	v_pk_fma_f32 v[20:21], v[44:45], v[46:47], v[20:21] op_sel_hi:[1,0,1] neg_lo:[1,0,0] neg_hi:[1,0,0]
	v_cndmask_b32_e32 v28, v24, v28, vcc
	v_cmp_gt_f32_e32 vcc, 0, v27
	v_lshl_add_u64 v[50:51], v[50:51], 0, v[108:109]
	v_cvt_pk_f16_f32 v24, v72, v73
	v_cndmask_b32_e32 v27, v25, v29, vcc
	v_cvt_pk_f16_f32 v25, v74, v75
	v_cvt_pk_f16_f32 v26, v30, v31
	v_cvt_pk_f16_f32 v27, v28, v27
	v_pk_fma_f32 v[20:21], v[46:47], v[20:21], v[40:41] op_sel:[1,0,0]
	global_store_dwordx4 v[50:51], v[24:27], off sc1
	v_pk_mul_f32 v[28:29], v[20:21], v[20:21]
	v_pk_fma_f32 v[22:23], v[84:85], v[46:47], v[22:23] op_sel_hi:[1,0,1]
	v_and_b32_e32 v25, 0x7fffffff, v21
	v_and_b32_e32 v24, 0x7fffffff, v20
	v_pk_fma_f32 v[24:25], v[24:25], s[18:19], 1.0 op_sel_hi:[1,0,0]
	v_pk_mul_f32 v[28:29], v[28:29], s[38:39] op_sel_hi:[1,0]
	v_rcp_f32_e32 v24, v24
	v_rcp_f32_e32 v25, v25
	v_pk_fma_f32 v[22:23], v[46:47], v[22:23], v[42:43] op_sel:[1,0,0]
	v_exp_f32_e32 v28, v28
	v_exp_f32_e32 v29, v29
	v_pk_fma_f32 v[26:27], v[24:25], s[26:27], v[62:63] op_sel_hi:[1,0,0]
	v_and_b32_e32 v31, 0x7fffffff, v23
	v_pk_fma_f32 v[26:27], v[24:25], v[26:27], s[30:31] op_sel_hi:[1,1,0]
	v_and_b32_e32 v30, 0x7fffffff, v22
	v_pk_fma_f32 v[26:27], v[24:25], v[26:27], s[34:35] op_sel_hi:[1,1,0]
	v_pk_fma_f32 v[30:31], v[30:31], s[18:19], 1.0 op_sel_hi:[1,0,0]
	v_pk_fma_f32 v[26:27], v[24:25], v[26:27], s[36:37] op_sel_hi:[1,1,0]
	v_rcp_f32_e32 v30, v30
	v_pk_mul_f32 v[24:25], v[24:25], v[26:27]
	v_rcp_f32_e32 v31, v31
	v_pk_mul_f32 v[24:25], v[28:29], v[24:25]
	v_cmp_gt_f32_e32 vcc, 0, v20
	v_pk_mul_f32 v[28:29], v[20:21], v[24:25]
	v_pk_fma_f32 v[24:25], v[20:21], v[24:25], v[20:21] neg_lo:[1,0,0] neg_hi:[1,0,0]
	v_pk_mul_f32 v[26:27], v[22:23], v[22:23]
	v_cndmask_b32_e32 v28, v24, v28, vcc
	v_cmp_gt_f32_e32 vcc, 0, v21
	v_pk_fma_f32 v[16:17], v[36:37], v[46:47], v[16:17] op_sel_hi:[1,0,1] neg_lo:[1,0,0] neg_hi:[1,0,0]
	v_pk_fma_f32 v[20:21], v[30:31], s[26:27], v[62:63] op_sel_hi:[1,0,0]
	v_cndmask_b32_e32 v29, v25, v29, vcc
	v_pk_mul_f32 v[24:25], v[26:27], s[38:39] op_sel_hi:[1,0]
	v_pk_fma_f32 v[16:17], v[46:47], v[16:17], v[32:33] op_sel:[1,0,0]
	v_pk_fma_f32 v[20:21], v[30:31], v[20:21], s[30:31] op_sel_hi:[1,1,0]
	v_exp_f32_e32 v24, v24
	v_exp_f32_e32 v25, v25
	v_pk_fma_f32 v[20:21], v[30:31], v[20:21], s[34:35] op_sel_hi:[1,1,0]
	v_and_b32_e32 v27, 0x7fffffff, v17
	v_and_b32_e32 v26, 0x7fffffff, v16
	v_pk_fma_f32 v[20:21], v[30:31], v[20:21], s[36:37] op_sel_hi:[1,1,0]
	v_pk_fma_f32 v[26:27], v[26:27], s[18:19], 1.0 op_sel_hi:[1,0,0]
	v_pk_mul_f32 v[20:21], v[30:31], v[20:21]
	v_rcp_f32_e32 v26, v26
	v_rcp_f32_e32 v27, v27
	v_pk_mul_f32 v[20:21], v[24:25], v[20:21]
	v_cmp_gt_f32_e32 vcc, 0, v22
	v_pk_mul_f32 v[24:25], v[22:23], v[20:21]
	v_pk_fma_f32 v[20:21], v[22:23], v[20:21], v[22:23] neg_lo:[1,0,0] neg_hi:[1,0,0]
	v_pk_fma_f32 v[18:19], v[38:39], v[46:47], v[18:19] op_sel_hi:[1,0,1]
	v_cndmask_b32_e32 v30, v20, v24, vcc
	v_cmp_gt_f32_e32 vcc, 0, v23
	v_pk_mul_f32 v[22:23], v[16:17], v[16:17]
	v_pk_fma_f32 v[18:19], v[46:47], v[18:19], v[34:35] op_sel:[1,0,0]
	v_cndmask_b32_e32 v31, v21, v25, vcc
	v_pk_fma_f32 v[20:21], v[26:27], s[26:27], v[62:63] op_sel_hi:[1,0,0]
	v_pk_mul_f32 v[22:23], v[22:23], s[38:39] op_sel_hi:[1,0]
	v_pk_fma_f32 v[20:21], v[26:27], v[20:21], s[30:31] op_sel_hi:[1,1,0]
	v_exp_f32_e32 v22, v22
	v_pk_fma_f32 v[20:21], v[26:27], v[20:21], s[34:35] op_sel_hi:[1,1,0]
	v_exp_f32_e32 v23, v23
	v_pk_fma_f32 v[20:21], v[26:27], v[20:21], s[36:37] op_sel_hi:[1,1,0]
	v_cmp_gt_f32_e32 vcc, 0, v16
	v_pk_mul_f32 v[20:21], v[26:27], v[20:21]
	v_and_b32_e32 v27, 0x7fffffff, v19
	v_and_b32_e32 v26, 0x7fffffff, v18
	v_pk_fma_f32 v[26:27], v[26:27], s[18:19], 1.0 op_sel_hi:[1,0,0]
	v_pk_mul_f32 v[20:21], v[22:23], v[20:21]
	v_rcp_f32_e32 v26, v26
	v_rcp_f32_e32 v27, v27
	v_pk_mul_f32 v[22:23], v[16:17], v[20:21]
	v_pk_fma_f32 v[20:21], v[16:17], v[20:21], v[16:17] neg_lo:[1,0,0] neg_hi:[1,0,0]
	v_pk_mul_f32 v[24:25], v[18:19], v[18:19]
	v_cndmask_b32_e32 v22, v20, v22, vcc
	v_cmp_gt_f32_e32 vcc, 0, v17
	v_pk_fma_f32 v[16:17], v[26:27], s[26:27], v[62:63] op_sel_hi:[1,0,0]
	v_pk_fma_f32 v[12:13], v[68:69], v[48:49], v[12:13] op_sel_hi:[1,0,1] neg_lo:[1,0,0] neg_hi:[1,0,0]
	v_cndmask_b32_e32 v23, v21, v23, vcc
	v_pk_mul_f32 v[20:21], v[24:25], s[38:39] op_sel_hi:[1,0]
	v_pk_fma_f32 v[16:17], v[26:27], v[16:17], s[30:31] op_sel_hi:[1,1,0]
	v_exp_f32_e32 v20, v20
	v_exp_f32_e32 v21, v21
	v_pk_fma_f32 v[16:17], v[26:27], v[16:17], s[34:35] op_sel_hi:[1,1,0]
	v_cmp_gt_f32_e32 vcc, 0, v18
	v_pk_fma_f32 v[16:17], v[26:27], v[16:17], s[36:37] op_sel_hi:[1,1,0]
	v_pk_fma_f32 v[12:13], v[48:49], v[12:13], v[64:65] op_sel:[1,0,0]
	v_pk_mul_f32 v[16:17], v[26:27], v[16:17]
	v_pk_fma_f32 v[14:15], v[92:93], v[48:49], v[14:15] op_sel_hi:[1,0,1]
	v_pk_mul_f32 v[16:17], v[20:21], v[16:17]
	v_pk_fma_f32 v[14:15], v[48:49], v[14:15], v[66:67] op_sel:[1,0,0]
	v_pk_mul_f32 v[20:21], v[18:19], v[16:17]
	v_pk_fma_f32 v[16:17], v[18:19], v[16:17], v[18:19] neg_lo:[1,0,0] neg_hi:[1,0,0]
	v_cvt_pk_f16_f32 v18, v22, v23
	v_cndmask_b32_e32 v20, v16, v20, vcc
	v_cmp_gt_f32_e32 vcc, 0, v19
	v_cvt_pk_f16_f32 v16, v28, v29
	v_pk_mul_f32 v[22:23], v[12:13], v[12:13]
	v_cndmask_b32_e32 v19, v17, v21, vcc
	v_cvt_pk_f16_f32 v17, v30, v31
	v_cvt_pk_f16_f32 v19, v20, v19
	global_store_dwordx4 v[50:51], v[16:19], off offset:256 sc1
	v_pk_mul_f32 v[22:23], v[22:23], s[38:39] op_sel_hi:[1,0]
	v_and_b32_e32 v25, 0x7fffffff, v15
	v_and_b32_e32 v19, 0x7fffffff, v13
	v_and_b32_e32 v18, 0x7fffffff, v12
	v_pk_fma_f32 v[18:19], v[18:19], s[18:19], 1.0 op_sel_hi:[1,0,0]
	v_exp_f32_e32 v22, v22
	v_rcp_f32_e32 v18, v18
	v_rcp_f32_e32 v19, v19
	v_exp_f32_e32 v23, v23
	v_and_b32_e32 v24, 0x7fffffff, v14
	v_pk_fma_f32 v[24:25], v[24:25], s[18:19], 1.0 op_sel_hi:[1,0,0]
	v_pk_fma_f32 v[20:21], v[18:19], s[26:27], v[62:63] op_sel_hi:[1,0,0]
	v_rcp_f32_e32 v24, v24
	v_pk_fma_f32 v[20:21], v[18:19], v[20:21], s[30:31] op_sel_hi:[1,1,0]
	v_rcp_f32_e32 v25, v25
	v_pk_fma_f32 v[20:21], v[18:19], v[20:21], s[34:35] op_sel_hi:[1,1,0]
	v_cmp_gt_f32_e32 vcc, 0, v12
	v_pk_fma_f32 v[20:21], v[18:19], v[20:21], s[36:37] op_sel_hi:[1,1,0]
	v_pk_fma_f32 v[8:9], v[60:61], v[48:49], v[8:9] op_sel_hi:[1,0,1] neg_lo:[1,0,0] neg_hi:[1,0,0]
	v_pk_mul_f32 v[18:19], v[18:19], v[20:21]
	v_pk_mul_f32 v[20:21], v[14:15], v[14:15]
	v_pk_mul_f32 v[18:19], v[22:23], v[18:19]
	v_pk_fma_f32 v[8:9], v[48:49], v[8:9], v[56:57] op_sel:[1,0,0]
	v_pk_mul_f32 v[22:23], v[12:13], v[18:19]
	v_pk_fma_f32 v[18:19], v[12:13], v[18:19], v[12:13] neg_lo:[1,0,0] neg_hi:[1,0,0]
	v_pk_fma_f32 v[10:11], v[70:71], v[48:49], v[10:11] op_sel_hi:[1,0,1]
	v_cndmask_b32_e32 v22, v18, v22, vcc
	v_cmp_gt_f32_e32 vcc, 0, v13
	v_pk_fma_f32 v[12:13], v[24:25], s[26:27], v[62:63] op_sel_hi:[1,0,0]
	v_pk_fma_f32 v[10:11], v[48:49], v[10:11], v[58:59] op_sel:[1,0,0]
	v_cndmask_b32_e32 v23, v19, v23, vcc
	v_pk_mul_f32 v[18:19], v[20:21], s[38:39] op_sel_hi:[1,0]
	v_pk_fma_f32 v[12:13], v[24:25], v[12:13], s[30:31] op_sel_hi:[1,1,0]
	v_exp_f32_e32 v18, v18
	v_exp_f32_e32 v19, v19
	v_pk_fma_f32 v[12:13], v[24:25], v[12:13], s[34:35] op_sel_hi:[1,1,0]
	v_and_b32_e32 v21, 0x7fffffff, v9
	v_and_b32_e32 v20, 0x7fffffff, v8
	v_pk_fma_f32 v[12:13], v[24:25], v[12:13], s[36:37] op_sel_hi:[1,1,0]
	v_pk_fma_f32 v[20:21], v[20:21], s[18:19], 1.0 op_sel_hi:[1,0,0]
	v_pk_mul_f32 v[12:13], v[24:25], v[12:13]
	v_rcp_f32_e32 v20, v20
	v_rcp_f32_e32 v21, v21
	v_pk_mul_f32 v[12:13], v[18:19], v[12:13]
	v_cmp_gt_f32_e32 vcc, 0, v14
	v_pk_mul_f32 v[18:19], v[14:15], v[12:13]
	v_pk_fma_f32 v[12:13], v[14:15], v[12:13], v[14:15] neg_lo:[1,0,0] neg_hi:[1,0,0]
	v_or_b32_e32 v16, 48, v135
	v_cndmask_b32_e32 v24, v12, v18, vcc
	v_cmp_gt_f32_e32 vcc, 0, v15
	v_pk_mul_f32 v[14:15], v[8:9], v[8:9]
	v_mad_i64_i32 v[16:17], s[42:43], v16, s63, 0
	v_cndmask_b32_e32 v25, v13, v19, vcc
	v_pk_fma_f32 v[12:13], v[20:21], s[26:27], v[62:63] op_sel_hi:[1,0,0]
	v_pk_mul_f32 v[14:15], v[14:15], s[38:39] op_sel_hi:[1,0]
	v_pk_fma_f32 v[12:13], v[20:21], v[12:13], s[30:31] op_sel_hi:[1,1,0]
	v_exp_f32_e32 v14, v14
	v_pk_fma_f32 v[12:13], v[20:21], v[12:13], s[34:35] op_sel_hi:[1,1,0]
	v_exp_f32_e32 v15, v15
	v_pk_fma_f32 v[12:13], v[20:21], v[12:13], s[36:37] op_sel_hi:[1,1,0]
	v_cmp_gt_f32_e32 vcc, 0, v8
	v_pk_mul_f32 v[12:13], v[20:21], v[12:13]
	v_and_b32_e32 v21, 0x7fffffff, v11
	v_and_b32_e32 v20, 0x7fffffff, v10
	v_pk_fma_f32 v[20:21], v[20:21], s[18:19], 1.0 op_sel_hi:[1,0,0]
	v_pk_mul_f32 v[12:13], v[14:15], v[12:13]
	v_rcp_f32_e32 v20, v20
	v_rcp_f32_e32 v21, v21
	v_pk_mul_f32 v[14:15], v[8:9], v[12:13]
	v_pk_fma_f32 v[12:13], v[8:9], v[12:13], v[8:9] neg_lo:[1,0,0] neg_hi:[1,0,0]
	v_pk_mul_f32 v[18:19], v[10:11], v[10:11]
	v_cndmask_b32_e32 v14, v12, v14, vcc
	v_cmp_gt_f32_e32 vcc, 0, v9
	v_pk_fma_f32 v[8:9], v[20:21], s[26:27], v[62:63] op_sel_hi:[1,0,0]
	v_lshl_add_u64 v[16:17], v[16:17], 1, s[8:9]
	v_cndmask_b32_e32 v15, v13, v15, vcc
	v_pk_mul_f32 v[12:13], v[18:19], s[38:39] op_sel_hi:[1,0]
	v_pk_fma_f32 v[8:9], v[20:21], v[8:9], s[30:31] op_sel_hi:[1,1,0]
	v_exp_f32_e32 v12, v12
	v_exp_f32_e32 v13, v13
	v_pk_fma_f32 v[8:9], v[20:21], v[8:9], s[34:35] op_sel_hi:[1,1,0]
	v_cmp_gt_f32_e32 vcc, 0, v10
	v_pk_fma_f32 v[8:9], v[20:21], v[8:9], s[36:37] op_sel_hi:[1,1,0]
	v_lshl_add_u64 v[16:17], v[16:17], 0, s[40:41]
	v_pk_mul_f32 v[8:9], v[20:21], v[8:9]
	v_pk_fma_f32 v[4:5], v[44:45], v[48:49], v[4:5] op_sel_hi:[1,0,1] neg_lo:[1,0,0] neg_hi:[1,0,0]
	v_pk_mul_f32 v[8:9], v[12:13], v[8:9]
	v_lshl_add_u64 v[16:17], v[16:17], 0, v[108:109]
	v_pk_mul_f32 v[12:13], v[10:11], v[8:9]
	v_pk_fma_f32 v[8:9], v[10:11], v[8:9], v[10:11] neg_lo:[1,0,0] neg_hi:[1,0,0]
	v_cvt_pk_f16_f32 v10, v14, v15
	v_cndmask_b32_e32 v12, v8, v12, vcc
	v_cmp_gt_f32_e32 vcc, 0, v11
	v_cvt_pk_f16_f32 v8, v22, v23
	v_pk_fma_f32 v[4:5], v[48:49], v[4:5], v[40:41] op_sel:[1,0,0]
	v_cndmask_b32_e32 v11, v9, v13, vcc
	v_cvt_pk_f16_f32 v9, v24, v25
	v_cvt_pk_f16_f32 v11, v12, v11
	global_store_dwordx4 v[16:17], v[8:11], off sc1
	v_pk_mul_f32 v[12:13], v[4:5], v[4:5]
	v_pk_fma_f32 v[6:7], v[84:85], v[48:49], v[6:7] op_sel_hi:[1,0,1]
	v_and_b32_e32 v9, 0x7fffffff, v5
	v_and_b32_e32 v8, 0x7fffffff, v4
	v_pk_fma_f32 v[8:9], v[8:9], s[18:19], 1.0 op_sel_hi:[1,0,0]
	v_pk_mul_f32 v[12:13], v[12:13], s[38:39] op_sel_hi:[1,0]
	v_rcp_f32_e32 v8, v8
	v_rcp_f32_e32 v9, v9
	v_pk_fma_f32 v[6:7], v[48:49], v[6:7], v[42:43] op_sel:[1,0,0]
	v_exp_f32_e32 v12, v12
	v_exp_f32_e32 v13, v13
	v_pk_fma_f32 v[10:11], v[8:9], s[26:27], v[62:63] op_sel_hi:[1,0,0]
	v_and_b32_e32 v15, 0x7fffffff, v7
	v_pk_fma_f32 v[10:11], v[8:9], v[10:11], s[30:31] op_sel_hi:[1,1,0]
	v_and_b32_e32 v14, 0x7fffffff, v6
	v_pk_fma_f32 v[10:11], v[8:9], v[10:11], s[34:35] op_sel_hi:[1,1,0]
	v_pk_fma_f32 v[14:15], v[14:15], s[18:19], 1.0 op_sel_hi:[1,0,0]
	v_pk_fma_f32 v[10:11], v[8:9], v[10:11], s[36:37] op_sel_hi:[1,1,0]
	v_rcp_f32_e32 v14, v14
	v_pk_mul_f32 v[8:9], v[8:9], v[10:11]
	v_rcp_f32_e32 v15, v15
	v_pk_mul_f32 v[8:9], v[12:13], v[8:9]
	v_cmp_gt_f32_e32 vcc, 0, v4
	v_pk_mul_f32 v[12:13], v[4:5], v[8:9]
	v_pk_fma_f32 v[8:9], v[4:5], v[8:9], v[4:5] neg_lo:[1,0,0] neg_hi:[1,0,0]
	v_pk_mul_f32 v[10:11], v[6:7], v[6:7]
	v_cndmask_b32_e32 v12, v8, v12, vcc
	v_cmp_gt_f32_e32 vcc, 0, v5
	v_pk_fma_f32 v[0:1], v[36:37], v[48:49], v[0:1] op_sel_hi:[1,0,1] neg_lo:[1,0,0] neg_hi:[1,0,0]
	v_pk_fma_f32 v[4:5], v[14:15], s[26:27], v[62:63] op_sel_hi:[1,0,0]
	v_cndmask_b32_e32 v13, v9, v13, vcc
	v_pk_mul_f32 v[8:9], v[10:11], s[38:39] op_sel_hi:[1,0]
	v_pk_fma_f32 v[0:1], v[48:49], v[0:1], v[32:33] op_sel:[1,0,0]
	v_pk_fma_f32 v[4:5], v[14:15], v[4:5], s[30:31] op_sel_hi:[1,1,0]
	v_exp_f32_e32 v8, v8
	v_exp_f32_e32 v9, v9
	v_pk_fma_f32 v[4:5], v[14:15], v[4:5], s[34:35] op_sel_hi:[1,1,0]
	v_and_b32_e32 v11, 0x7fffffff, v1
	v_and_b32_e32 v10, 0x7fffffff, v0
	v_pk_fma_f32 v[4:5], v[14:15], v[4:5], s[36:37] op_sel_hi:[1,1,0]
	v_pk_fma_f32 v[10:11], v[10:11], s[18:19], 1.0 op_sel_hi:[1,0,0]
	v_pk_mul_f32 v[4:5], v[14:15], v[4:5]
	v_rcp_f32_e32 v10, v10
	v_rcp_f32_e32 v11, v11
	v_pk_mul_f32 v[4:5], v[8:9], v[4:5]
	v_cmp_gt_f32_e32 vcc, 0, v6
	v_pk_mul_f32 v[8:9], v[6:7], v[4:5]
	v_pk_fma_f32 v[4:5], v[6:7], v[4:5], v[6:7] neg_lo:[1,0,0] neg_hi:[1,0,0]
	v_pk_fma_f32 v[2:3], v[38:39], v[48:49], v[2:3] op_sel_hi:[1,0,1]
	v_cndmask_b32_e32 v14, v4, v8, vcc
	v_cmp_gt_f32_e32 vcc, 0, v7
	v_pk_mul_f32 v[6:7], v[0:1], v[0:1]
	v_pk_fma_f32 v[2:3], v[48:49], v[2:3], v[34:35] op_sel:[1,0,0]
	v_cndmask_b32_e32 v15, v5, v9, vcc
	v_pk_fma_f32 v[4:5], v[10:11], s[26:27], v[62:63] op_sel_hi:[1,0,0]
	v_pk_mul_f32 v[6:7], v[6:7], s[38:39] op_sel_hi:[1,0]
	v_pk_fma_f32 v[4:5], v[10:11], v[4:5], s[30:31] op_sel_hi:[1,1,0]
	v_exp_f32_e32 v6, v6
	v_pk_fma_f32 v[4:5], v[10:11], v[4:5], s[34:35] op_sel_hi:[1,1,0]
	v_exp_f32_e32 v7, v7
	v_pk_fma_f32 v[4:5], v[10:11], v[4:5], s[36:37] op_sel_hi:[1,1,0]
	v_cmp_gt_f32_e32 vcc, 0, v0
	v_pk_mul_f32 v[4:5], v[10:11], v[4:5]
	v_and_b32_e32 v11, 0x7fffffff, v3
	v_and_b32_e32 v10, 0x7fffffff, v2
	v_pk_fma_f32 v[10:11], v[10:11], s[18:19], 1.0 op_sel_hi:[1,0,0]
	v_pk_mul_f32 v[4:5], v[6:7], v[4:5]
	v_rcp_f32_e32 v10, v10
	v_rcp_f32_e32 v11, v11
	v_pk_mul_f32 v[6:7], v[0:1], v[4:5]
	v_pk_fma_f32 v[4:5], v[0:1], v[4:5], v[0:1] neg_lo:[1,0,0] neg_hi:[1,0,0]
	v_pk_mul_f32 v[8:9], v[2:3], v[2:3]
	v_cndmask_b32_e32 v6, v4, v6, vcc
	v_cmp_gt_f32_e32 vcc, 0, v1
	v_pk_fma_f32 v[0:1], v[10:11], s[26:27], v[62:63] op_sel_hi:[1,0,0]
	s_mov_b64 s[42:43], s[4:5]
	v_cndmask_b32_e32 v7, v5, v7, vcc
	v_pk_mul_f32 v[4:5], v[8:9], s[38:39] op_sel_hi:[1,0]
	v_pk_fma_f32 v[0:1], v[10:11], v[0:1], s[30:31] op_sel_hi:[1,1,0]
	v_exp_f32_e32 v4, v4
	v_exp_f32_e32 v5, v5
	v_pk_fma_f32 v[0:1], v[10:11], v[0:1], s[34:35] op_sel_hi:[1,1,0]
	v_cmp_gt_f32_e32 vcc, 0, v2
	v_pk_fma_f32 v[0:1], v[10:11], v[0:1], s[36:37] op_sel_hi:[1,1,0]
	s_mov_b64 s[40:41], s[6:7]
	v_pk_mul_f32 v[0:1], v[10:11], v[0:1]
	s_nop 0
	v_pk_mul_f32 v[0:1], v[4:5], v[0:1]
	s_nop 0
	v_pk_mul_f32 v[4:5], v[2:3], v[0:1]
	v_pk_fma_f32 v[0:1], v[2:3], v[0:1], v[2:3] neg_lo:[1,0,0] neg_hi:[1,0,0]
	v_cvt_pk_f16_f32 v2, v6, v7
	v_cndmask_b32_e32 v4, v0, v4, vcc
	v_cmp_gt_f32_e32 vcc, 0, v3
	v_cvt_pk_f16_f32 v0, v12, v13
	s_nop 0
	v_cndmask_b32_e32 v3, v1, v5, vcc
	v_cvt_pk_f16_f32 v1, v14, v15
	v_cvt_pk_f16_f32 v3, v4, v3
	s_and_b64 vcc, exec, s[0:1]
	global_store_dwordx4 v[16:17], v[0:3], off offset:256 sc1
	s_cbranch_vccnz .LBB5_56
